# speedup vs baseline: 1.1565x; 1.0014x over previous
.LBB5_15:
	s_or_b64 exec, exec, s[6:7]
	s_load_dwordx4 s[4:7], s[0:1], 0x18
	v_mov_b32_e32 v17, 0
	s_waitcnt lgkmcnt(0)
	s_barrier
	ds_read_b32 v17, v17 offset:32776
	s_and_b32 s17, s5, 0xffff
	s_and_b32 s21, s15, 0xffff
	v_accvgpr_read_b32 v56, a0
	v_lshlrev_b32_e32 v15, 12, v1
	v_lshlrev_b32_e32 v18, 4, v56
	s_add_u32 s8, s4, s7
	s_mov_b32 s16, s4
	v_lshlrev_b32_e32 v14, 14, v10
	v_lshlrev_b32_e32 v16, 7, v0
	s_addc_u32 s9, s5, 0
	s_waitcnt lgkmcnt(0)
	v_cmp_ne_u32_e64 s[4:5], 0, v17
	v_add_u32_e32 v17, 0, v15
	v_or_b32_e32 v15, v18, v15
	v_or3_b32 v15, v16, v14, v15
	v_lshlrev_b32_e32 v13, 3, v0
	v_accvgpr_write_b32 a98, v15
	v_and_b32_e32 v15, 63, v57
	v_lshlrev_b32_e32 v19, 4, v13
	v_lshrrev_b32_e32 v15, 5, v15
	s_waitcnt vmcnt(1)
	v_mul_f32_e32 v45, 0xbfb8aa3b, v6
	v_mul_f32_e32 v6, 0xbfb8aa3b, v7
	v_mul_f32_e32 v7, 0xbfb8aa3b, v9
	v_lshlrev_b32_e32 v9, 8, v1
	v_add3_u32 v17, v17, v19, v18
	v_accvgpr_write_b32 a94, v15
	v_bfe_u32 v16, v57, 2, 3
	v_lshlrev_b32_e32 v15, 3, v57
	v_add_u32_e32 v9, v23, v9
	v_accvgpr_write_b32 a97, v17
	v_and_b32_e32 v17, 24, v15
	v_lshlrev_b32_e32 v10, 13, v10
	v_lshlrev_b32_e32 v15, 10, v16
	v_or_b32_e32 v9, v9, v13
	v_or3_b32 v10, v10, v15, v17
	v_cmp_eq_u32_e64 s[2:3], 3, v1
	v_lshl_add_u32 v9, v9, 1, s6
	v_accvgpr_write_b32 a95, v16
	v_lshl_add_u32 v16, v10, 1, s44
	v_lshlrev_b32_e32 v1, 7, v1
	v_and_b32_e32 v10, 8, v57
	v_lshlrev_b32_e32 v0, 1, v0
	v_or3_b32 v1, v1, v10, v0
	v_add_u32_e32 v10, s24, v9
	s_lshl_b32 s6, s33, 9
	v_or3_b32 v1, v1, v18, v14
	v_accvgpr_write_b32 a99, v10
	v_add_u32_e32 v10, s26, v9
	v_add_u32_e32 v1, s6, v1
	s_and_b32 s33, s6, 0xe00
	s_lshl_b32 s6, s42, 9
	v_accvgpr_write_b32 a102, v10
	v_add_u32_e32 v10, s28, v9
	s_and_b32 s35, s6, 0xe00
	s_lshl_b32 s6, s43, 9
	v_accvgpr_write_b32 a103, v10
	v_add_u32_e32 v10, s30, v9
	s_and_b32 s37, s6, 0xe00
	s_lshl_b32 s6, s45, 9
	v_accvgpr_write_b32 a104, v10
	v_add_u32_e32 v10, s34, v9
	v_accvgpr_write_b32 a96, v17
	v_ashrrev_i32_e32 v17, 31, v16
	s_and_b32 s39, s6, 0xe00
	s_lshl_b32 s6, s46, 9
	v_accvgpr_write_b32 a105, v10
	v_add_u32_e32 v10, s36, v9
	v_accvgpr_write_b32 a93, v17
	s_and_b32 s41, s6, 0xe00
	s_lshl_b32 s6, s47, 9
	v_accvgpr_write_b32 a106, v10
	v_add_u32_e32 v10, s38, v9
	v_add_u32_e32 v9, s40, v9
	v_or_b32_e32 v13, v13, v56
	v_accvgpr_write_b32 a92, v16
	v_lshl_add_u64 v[16:17], s[8:9], 0, v[16:17]
	s_and_b32 s42, s6, 0xe00
	s_lshl_b32 s6, s48, 9
	v_accvgpr_write_b32 a108, v9
	v_lshlrev_b32_e32 v9, 1, v12
	s_mov_b32 s19, 0x20000
	v_accvgpr_write_b32 a101, v17
	s_and_b32 s43, s6, 0xe00
	s_lshl_b32 s6, s49, 9
	v_accvgpr_write_b32 a107, v10
	v_add3_u32 v0, 0, v9, v0
	v_lshlrev_b32_e32 v9, 9, v11
	v_lshlrev_b32_e32 v10, 4, v13
	s_brev_b32 s18, -2
	s_mov_b32 s22, 0x80000
	s_mov_b32 s23, s19
	s_mov_b32 s20, s14
	v_cmp_gt_u32_e64 s[0:1], 8, v22
	s_mov_b32 s15, 0
	v_accvgpr_write_b32 a100, v16
	s_and_b32 s44, s6, 0xe00
	v_add3_u32 v9, 0, v9, v10
	s_mov_b64 s[26:27], 0
	s_mov_b32 s34, 0x80008000
	s_mov_b32 s36, 0x100000
	s_brev_b32 s38, 60
	s_mov_b32 s40, 0xbc38aa3b
	s_mov_b32 s45, 0x41000000
	s_waitcnt vmcnt(0)
	v_accvgpr_write_b32 a112, v250
	v_accvgpr_write_b32 a113, v251
	v_accvgpr_write_b32 a114, v252
	v_accvgpr_write_b32 a115, v253
	v_accvgpr_write_b32 a116, v2
	v_accvgpr_write_b32 a117, v3
	v_accvgpr_write_b32 a118, v4
	v_accvgpr_write_b32 a119, v5
	v_and_b32_e32 v46, 2, v57
	v_cmp_ne_u32_e64 s[0:1], 0, v46
	v_and_b32_e32 v46, 32, v57
	v_cmp_ne_u32_e64 s[30:31], 0, v46
	v_mov_b32_e32 v26, 0x44444444
	v_mov_b32_e32 v46, 0xeeeeeeee
	v_cndmask_b32_e64 v26, v26, v46, s[0:1]
	v_accvgpr_read_b32 v46, a98
	v_bfe_u32 v47, v57, 4, 2
	v_lshlrev_b32_e32 v47, 7, v47
	v_sub_u32_e32 v46, v46, v47
	v_and_b32_e32 v47, 7, v57
	v_lshlrev_b32_e32 v47, 4, v47
	v_sub_u32_e32 v46, v46, v47
	v_bfe_u32 v47, v57, 4, 1
	v_lshl_add_u32 v46, v47, 8, v46
	v_and_b32_e32 v47, 15, v57
	v_lshl_add_u32 v46, v47, 4, v46
	v_mov_b32_e32 v47, s33
	v_mov_b32_e32 v48, s35
	v_cndmask_b32_e64 v47, v47, v48, s[30:31]
	v_or_b32_e32 v27, v46, v47
	v_mov_b32_e32 v47, s37
	v_mov_b32_e32 v48, s39
	v_cndmask_b32_e64 v47, v47, v48, s[30:31]
	v_or_b32_e32 v28, v46, v47
	v_mov_b32_e32 v47, s41
	v_mov_b32_e32 v48, s42
	v_cndmask_b32_e64 v47, v47, v48, s[30:31]
	v_or_b32_e32 v29, v46, v47
	v_mov_b32_e32 v47, s43
	v_mov_b32_e32 v48, s44
	v_cndmask_b32_e64 v47, v47, v48, s[30:31]
	v_or_b32_e32 v30, v46, v47
	v_lshrrev_b32_e32 v46, 6, v57
	v_lshlrev_b32_e32 v46, 7, v46
	v_and_b32_e32 v47, 8, v57
	v_bfe_u32 v48, v57, 4, 2
	v_lshl_or_b32 v47, v48, 1, v47
	v_add_u32_e32 v46, v46, v47
	v_and_b32_e32 v47, 7, v57
	v_lshl_add_u32 v46, v47, 4, v46
	v_sub_u32_e32 v1, v1, v46
	v_bfe_u32 v46, v57, 7, 1
	v_lshlrev_b32_e32 v46, 8, v46
	v_bfe_u32 v47, v57, 1, 2
	v_lshl_or_b32 v46, v47, 6, v46
	v_bfe_u32 v47, v57, 5, 1
	v_lshl_or_b32 v46, v47, 5, v46
	v_and_b32_e32 v47, 1, v57
	v_lshl_or_b32 v46, v47, 4, v46
	v_bfe_u32 v47, v57, 3, 1
	v_bfe_u32 v48, v57, 6, 1
	v_lshl_or_b32 v47, v48, 1, v47
	v_lshl_or_b32 v46, v47, 2, v46
	v_bfe_u32 v47, v57, 4, 1
	v_lshl_or_b32 v46, v47, 1, v46
	v_add_u32_e32 v1, v1, v46
	v_lshrrev_b32_e32 v46, 6, v57
	v_lshlrev_b32_e32 v46, 12, v46
	v_bfe_u32 v47, v57, 4, 2
	v_lshl_or_b32 v46, v47, 10, v46
	v_and_b32_e32 v47, 3, v57
	v_lshl_or_b32 v46, v47, 2, v46
	v_bfe_u32 v47, v57, 3, 1
	v_bfe_u32 v48, v57, 4, 1
	v_xor_b32_e32 v47, v47, v48
	v_lshl_or_b32 v46, v47, 5, v46
	v_bfe_u32 v47, v57, 5, 1
	v_lshl_or_b32 v46, v47, 7, v46
	v_bfe_u32 v47, v57, 2, 1
	v_lshl_or_b32 v31, v47, 4, v46
	v_xor_b32_e32 v32, 0x80, v31
	v_xor_b32_e32 v47, 1, v47
	v_lshl_or_b32 v33, v47, 4, v46
	v_add_u32_e32 v33, 0x200, v33
	v_xor_b32_e32 v34, 0x80, v33
	v_lshrrev_b32_e32 v46, 3, v57
	v_and_b32_e32 v46, 24, v46
	v_lshrrev_b32_e32 v47, 1, v57
	v_and_or_b32 v46, v47, 4, v46
	v_bfe_u32 v47, v57, 4, 2
	v_or_b32_e32 v46, v46, v47
	v_and_b32_e32 v47, 3, v57
	v_and_b32_e32 v48, 4, v57
	v_lshl_or_b32 v47, v48, 1, v47
	v_xor_b32_e32 v46, v46, v47
	v_and_b32_e32 v47, 7, v57
	v_lshlrev_b32_e32 v47, 9, v47
	v_lshl_or_b32 v9, v46, 4, v47
	v_accvgpr_write_b32 a120, v226
	v_accvgpr_write_b32 a121, v227
	v_accvgpr_write_b32 a122, v228
	v_accvgpr_write_b32 a123, v229
	v_accvgpr_write_b32 a124, v230
	v_accvgpr_write_b32 a125, v231
	v_accvgpr_write_b32 a126, v232
	v_accvgpr_write_b32 a127, v233
	v_accvgpr_write_b32 a128, v234
	v_accvgpr_write_b32 a129, v235
	v_accvgpr_write_b32 a130, v236
	v_accvgpr_write_b32 a131, v237
	v_accvgpr_write_b32 a132, v238
	v_accvgpr_write_b32 a133, v239
	v_accvgpr_write_b32 a134, v240
	v_accvgpr_write_b32 a135, v241
	v_accvgpr_write_b32 a136, v242
	v_accvgpr_write_b32 a137, v243
	v_accvgpr_write_b32 a138, v244
	v_accvgpr_write_b32 a139, v245
	v_accvgpr_write_b32 a140, v246
	v_accvgpr_write_b32 a141, v247
	v_accvgpr_write_b32 a142, v248
	v_accvgpr_write_b32 a143, v249
	v_accvgpr_write_b32 a144, v194
	v_accvgpr_write_b32 a145, v195
	v_accvgpr_write_b32 a146, v196
	v_accvgpr_write_b32 a147, v197
	v_accvgpr_write_b32 a148, v198
	v_accvgpr_write_b32 a149, v199
	v_accvgpr_write_b32 a150, v200
	v_accvgpr_write_b32 a151, v201
	v_accvgpr_write_b32 a152, v202
	v_accvgpr_write_b32 a153, v203
	v_accvgpr_write_b32 a154, v204
	v_accvgpr_write_b32 a155, v205
	v_accvgpr_write_b32 a156, v206
	v_accvgpr_write_b32 a157, v207
	v_accvgpr_write_b32 a158, v208
	v_accvgpr_write_b32 a159, v209
	v_accvgpr_write_b32 a160, v210
	v_accvgpr_write_b32 a161, v211
	v_accvgpr_write_b32 a162, v212
	v_accvgpr_write_b32 a163, v213
	v_accvgpr_write_b32 a164, v214
	v_accvgpr_write_b32 a165, v215
	v_accvgpr_write_b32 a166, v216
	v_accvgpr_write_b32 a167, v217
	v_accvgpr_write_b32 a168, v218
	v_accvgpr_write_b32 a169, v219
	v_accvgpr_write_b32 a170, v220
	v_accvgpr_write_b32 a171, v221
	v_accvgpr_write_b32 a172, v222
	v_accvgpr_write_b32 a173, v223
	v_accvgpr_write_b32 a174, v224
	v_accvgpr_write_b32 a175, v225
	s_mov_b64 s[24:25], 0
	s_mov_b32 s46, 0
	s_mov_b32 s30, 0x3c38aa3b
	s_mov_b32 s31, 0xbc000000
	v_bfe_u32 v50, v57, 4, 2
	v_lshlrev_b32_e32 v50, 4, v50
	v_bfe_u32 v51, v57, 4, 1
	v_bfe_u32 v52, v57, 1, 1
	v_lshlrev_b32_e32 v52, 2, v52
	v_lshl_or_b32 v51, v51, 5, v52
	v_sub_u32_e32 v54, v51, v50
	v_bfe_u32 v51, v57, 2, 2
	v_and_b32_e32 v52, 1, v57
	v_lshl_or_b32 v51, v51, 1, v52
	v_and_b32_e32 v52, 7, v57
	v_sub_u32_e32 v51, v51, v52
	v_lshlrev_b32_e32 v51, 11, v51
	v_add_u32_e32 v54, v54, v51
	v_and_b32_e32 v55, 32, v57
	v_cmp_ne_u32_e64 s[28:29], 0, v55
	v_accvgpr_read_b32 v242, a99
	v_accvgpr_read_b32 v55, a102
	v_cndmask_b32_e64 v242, v242, v55, s[28:29]
	v_add_u32_e32 v242, v242, v54
	v_accvgpr_read_b32 v243, a103
	v_accvgpr_read_b32 v55, a104
	v_cndmask_b32_e64 v243, v243, v55, s[28:29]
	v_add_u32_e32 v243, v243, v54
	v_accvgpr_read_b32 v244, a105
	v_accvgpr_read_b32 v55, a106
	v_cndmask_b32_e64 v244, v244, v55, s[28:29]
	v_add_u32_e32 v244, v244, v54
	v_accvgpr_read_b32 v245, a107
	v_accvgpr_read_b32 v55, a108
	v_cndmask_b32_e64 v245, v245, v55, s[28:29]
	v_add_u32_e32 v245, v245, v54
	s_mov_b64 s[26:27], -1
	v_mov_b32_e32 v10, 0
	v_mov_b32_e32 v11, 0
	v_mov_b32_e32 v12, 0
	v_mov_b32_e32 v13, 0
	v_mov_b32_e32 v14, 0
	v_mov_b32_e32 v15, 0
	v_mov_b32_e32 v16, 0
	v_mov_b32_e32 v17, 0
	v_mov_b32_e32 v18, 0
	v_mov_b32_e32 v19, 0
	v_mov_b32_e32 v20, 0
	v_mov_b32_e32 v21, 0
	v_mov_b32_e32 v22, 0
	v_mov_b32_e32 v23, 0
	v_mov_b32_e32 v24, 0
	v_mov_b32_e32 v25, 0
	v_mov_b32_e32 v2, 0
	v_mov_b32_e32 v3, 0
	v_mov_b32_e32 v4, 0
	v_mov_b32_e32 v5, 0
	v_mov_b32_e32 v250, 0
	v_mov_b32_e32 v251, 0
	v_mov_b32_e32 v252, 0
	v_mov_b32_e32 v253, 0
	v_mov_b32_e32 v46, 0
	v_mov_b32_e32 v47, 0
	v_mov_b32_e32 v48, 0
	v_mov_b32_e32 v49, 0
	v_mov_b32_e32 v50, 0
	v_mov_b32_e32 v51, 0
	v_mov_b32_e32 v52, 0
	v_mov_b32_e32 v53, 0
	buffer_load_dword v226, v242, s[16:19], 0 offen sc1
	buffer_load_dword v227, v242, s[16:19], 0 offen offset:8 sc1
	buffer_load_dword v228, v242, s[16:19], 0 offen offset:16 sc1
	buffer_load_dword v229, v242, s[16:19], 0 offen offset:24 sc1
	buffer_load_dword v230, v243, s[16:19], 0 offen sc1
	buffer_load_dword v231, v243, s[16:19], 0 offen offset:8 sc1
	buffer_load_dword v232, v243, s[16:19], 0 offen offset:16 sc1
	buffer_load_dword v233, v243, s[16:19], 0 offen offset:24 sc1
	buffer_load_dword v234, v244, s[16:19], 0 offen sc1
	buffer_load_dword v235, v244, s[16:19], 0 offen offset:8 sc1
	buffer_load_dword v236, v244, s[16:19], 0 offen offset:16 sc1
	buffer_load_dword v237, v244, s[16:19], 0 offen offset:24 sc1
	buffer_load_dword v238, v245, s[16:19], 0 offen sc1
	buffer_load_dword v239, v245, s[16:19], 0 offen offset:8 sc1
	buffer_load_dword v240, v245, s[16:19], 0 offen offset:16 sc1
	buffer_load_dword v241, v245, s[16:19], 0 offen offset:24 sc1
	s_waitcnt vmcnt(0)

.Lrec_tail:
	s_add_i32 s14, s46, 1
	s_lshl_b32 s6, s14, 13
	s_lshl_b32 s7, s14, 17
	s_and_b32 s6, s6, 0x8000
	s_and_b32 s7, s7, 0x60000
	v_pk_add_f32 v[10:11], v[10:11], v[12:13]
	v_pk_add_f32 v[14:15], v[14:15], v[16:17]
	ds_write2_b32 v31, v10, v14 offset0:0 offset1:16
	ds_write2_b32 v33, v11, v15 offset0:0 offset1:16
	v_pk_add_f32 v[18:19], v[18:19], v[20:21]
	v_pk_add_f32 v[22:23], v[22:23], v[24:25]
	ds_write2_b32 v32, v18, v22 offset0:0 offset1:16
	ds_write2_b32 v34, v19, v23 offset0:0 offset1:16
	v_pk_add_f32 v[46:47], v[46:47], v[48:49]
	v_pk_add_f32 v[50:51], v[50:51], v[52:53]
	ds_write2_b32 v31, v46, v50 offset0:64 offset1:80
	ds_write2_b32 v33, v47, v51 offset0:64 offset1:80
	v_pk_add_f32 v[2:3], v[2:3], v[4:5]
	v_pk_add_f32 v[250:251], v[250:251], v[252:253]
	ds_write2_b32 v32, v2, v250 offset0:64 offset1:80
	ds_write2_b32 v34, v3, v251 offset0:64 offset1:80
	s_waitcnt lgkmcnt(0)
	s_barrier
	ds_read_b128 v[10:13], v9
	ds_read_b128 v[14:17], v9 offset:4096
	ds_read_b128 v[18:21], v9 offset:8192
	ds_read_b128 v[22:25], v9 offset:12288
	s_min_u32 s29, s46, 0xfd
	s_lshl_b32 s29, s29, 19
	s_add_u32 s29, s29, s36
	v_mov_b32_e32 v54, s29
	v_add_co_u32_e32 v54, vcc, v254, v54
	s_nop 1
	v_addc_co_u32_e32 v55, vcc, 0, v255, vcc
	global_load_dwordx2 v[40:41], v[54:55], off
	s_waitcnt lgkmcnt(2)
	v_pk_add_f32 v[10:11], v[10:11], v[14:15]
	v_pk_add_f32 v[12:13], v[12:13], v[16:17]
	s_waitcnt lgkmcnt(0)
	v_pk_add_f32 v[18:19], v[18:19], v[22:23]
	v_pk_add_f32 v[20:21], v[20:21], v[24:25]
	v_pk_add_f32 v[10:11], v[10:11], v[18:19]
	v_pk_add_f32 v[12:13], v[12:13], v[20:21]
	v_fmac_f32_e32 v247, s48, v11
	v_fmac_f32_e32 v246, s48, v10
	v_fmac_f32_e32 v249, s48, v13
	v_fmac_f32_e32 v248, s47, v12
	v_exp_f32_e32 v15, v247
	v_exp_f32_e32 v14, v246
	v_exp_f32_e32 v17, v249
	v_max_f32_e32 v16, 0, v248
	v_add_f32_e32 v15, 1.0, v15
	v_add_f32_e32 v14, 1.0, v14
	v_add_f32_e32 v17, 1.0, v17
	v_rcp_f32_e32 v14, v14
	v_rcp_f32_e32 v15, v15
	v_rcp_f32_e32 v17, v17
	v_add_u32_e32 v18, s7, v1
	v_mul_f32_e32 v12, v16, v14
	v_fmac_f32_e32 v12, v44, v15
	v_max_f32_e32 v19, 0, v12
	v_mul_f32_e32 v13, v17, v19
	v_fma_mixlo_f16 v14, v13, s45, 0
	s_lshl_b32 s29, s46, 3
	v_and_b32_e32 v14, 0x7fff, v14
	s_andn2_b64 vcc, exec, s[4:5]
	v_or_b32_e32 v16, s6, v14
	s_cbranch_vccnz .Lrec_slowst
	buffer_store_short v16, v18, s[20:23], 0 offen
	s_branch .Lrec_stored
